# row-scale loads hoisted in P10 and P11 epilogues only (no code placement pads)
# speedup vs baseline: 1.0110x; 1.0110x over previous
;     __device__ __forceinline__ void operator()(const f32x4 (&acc)[2][2][4][2], const Unit& u, int wr, int wc, int fr, int fq) const {
;         const int row0 = u.pm * BM + wr * 64 + fr, j0 = u.pn * HALF + wc * 32 + 8 * fq;
;         const float* bg = bgu + (size_t)u.e * 2 * DFF + j0;
;         f32x4 bgv[2], buv[2];
; #pragma unroll
;         for (int n = 0; n < 2; ++n) { bgv[n] = *(const f32x4*)(bg + 4 * n); buv[n] = *(const f32x4*)(bg + DFF + 4 * n); }
;         constexpr float inv = 1.0f / W8_SCALE;
; #pragma unroll
;         for (int ai = 0; ai < 2; ++ai)
; #pragma unroll
;             for (int m = 0; m < 4; ++m) { const int r = row0 + ai * HALF + m * 16; unsigned char* rowp = O + (size_t)r * DFF + j0; const float sc = inv * rs[(size_t)u.e * XCAP + u.lr0 + (r - u.pm * BM)];
;                 float a[8];
; #pragma unroll
;                 for (int n = 0; n < 2; ++n)
; #pragma unroll
;                     for (int h = 0; h < 2; ++h) {
;                         const f32x2 ag = {acc[ai][0][m][n][2 * h], acc[ai][0][m][n][2 * h + 1]}, au = {acc[ai][1][m][n][2 * h], acc[ai][1][m][n][2 * h + 1]};
;                         const f32x2 bg2 = {bgv[n][2 * h], bgv[n][2 * h + 1]}, bu2 = {buv[n][2 * h], buv[n][2 * h + 1]};
;                         f32x2 g = ag * sc + bg2, up = au * sc + bu2;
;                         g.x = fminf(g.x, 7.0f); g.y = fminf(g.y, 7.0f);
;                         up.x = __builtin_amdgcn_fmed3f(up.x, -7.0f, 7.0f); up.y = __builtin_amdgcn_fmed3f(up.y, -7.0f, 7.0f);
;                         const f32x2 t = g * (-1.702f * 1.4426950408889634f);
;                         f32x2 e; e.x = __builtin_amdgcn_exp2f(t.x); e.y = __builtin_amdgcn_exp2f(t.y);
;                         const f32x2 d = e + 1.0f;
;                         f32x2 rr; rr.x = __builtin_amdgcn_rcpf(d.x); rr.y = __builtin_amdgcn_rcpf(d.y);
;                         const f32x2 o2 = (up * ACT8_SCALE + ACT8_SCALE) * (g * rr);
;                         a[4 * n + 2 * h] = o2.x; a[4 * n + 2 * h + 1] = o2.y; }
;                 u32x2 w; w.x = cvt_pk4_fp8(a[0], a[1], a[2], a[3]); w.y = cvt_pk4_fp8(a[4], a[5], a[6], a[7]);
;                 *(u32x2*)rowp = w; }
.LBB0_1062:
	s_lshl_b32 s39, s50, 7
	s_ashr_i32 s49, s48, 31
	s_lshl_b32 s35, s35, 8
	s_or_b32 s39, s39, s84
	s_lshl_b64 s[54:55], s[48:49], 14
	v_mbcnt_lo_u32_b32 v80, -1, 0
	v_mbcnt_hi_u32_b32 v80, -1, v80
	s_add_u32 s54, s6, s54
	v_ashrrev_i32_e32 v81, 1, v80
	v_and_b32_e32 v81, -8, v81
	s_addc_u32 s55, s7, s55
	s_ashr_i32 s53, s52, 31
	s_lshl_b64 s[48:49], s[48:49], 16
	v_add_u32_e32 v148, s39, v81
	s_add_u32 s39, s26, s48
	s_addc_u32 s43, s27, s49
	s_lshl_b64 s[48:49], s[52:53], 2
	v_ashrrev_i32_e32 v149, 31, v148
	v_and_or_b32 v144, v80, 15, s34
	s_add_u32 s48, s39, s48
	v_lshl_add_u64 v[88:89], v[148:149], 2, s[54:55]
	s_addc_u32 s49, s43, s49
	v_lshlrev_b32_e32 v80, 2, v144
	s_movk_i32 s39, 0x2000
	global_load_dword v164, v80, s[48:49]
	global_load_dword v240, v80, s[48:49] offset:64
	global_load_dword v241, v80, s[48:49] offset:128
	global_load_dword v242, v80, s[48:49] offset:192
	global_load_dword v243, v80, s[48:49] offset:512
	global_load_dword v244, v80, s[48:49] offset:576
	global_load_dword v245, v80, s[48:49] offset:640
	global_load_dword v246, v80, s[48:49] offset:704
	v_add_co_u32_e32 v80, vcc, s39, v88
	s_mov_b64 s[52:53], 0x2000
	s_nop 0
	v_addc_co_u32_e32 v81, vcc, 0, v89, vcc
	global_load_dwordx4 v[84:87], v[80:81], off
	global_load_dwordx4 v[92:95], v[88:89], off
	s_nop 0
	global_load_dwordx4 v[80:83], v[88:89], off offset:16
	v_lshl_add_u64 v[88:89], v[88:89], 0, s[52:53]
	global_load_dwordx4 v[88:91], v[88:89], off offset:16
	v_add_u32_e32 v150, s35, v144
	v_ashrrev_i32_e32 v151, 31, v150
	v_mov_b32_e32 v162, v145
	v_mov_b32_e32 v163, v145
	v_lshlrev_b64 v[146:147], 11, v[150:151]
	s_ashr_i32 s39, s35, 31
	v_lshl_add_u64 v[146:147], s[4:5], 0, v[146:147]
	v_mov_b32_e32 v172, s39
	v_lshl_add_u64 v[146:147], v[146:147], 0, v[148:149]
	s_waitcnt vmcnt(4)
	v_mul_f32_e32 v144, 0x3c800000, v164
	s_waitcnt vmcnt(3)
	v_pk_fma_f32 v[132:133], v[132:133], v[144:145], v[84:85] op_sel_hi:[1,0,1]
	s_waitcnt vmcnt(2)
	v_pk_fma_f32 v[140:141], v[140:141], v[144:145], v[92:93] op_sel_hi:[1,0,1]
	s_waitcnt vmcnt(1)
	v_pk_fma_f32 v[136:137], v[136:137], v[144:145], v[80:81] op_sel_hi:[1,0,1]
	v_min_f32_e32 v140, 0x40e00000, v140
	v_min_f32_e32 v141, 0x40e00000, v141
	v_min_f32_e32 v136, 0x40e00000, v136
	v_min_f32_e32 v137, 0x40e00000, v137
	v_pk_mul_f32 v[164:165], v[140:141], s[36:37] op_sel_hi:[1,0]
	v_pk_mul_f32 v[168:169], v[136:137], s[36:37] op_sel_hi:[1,0]
	v_exp_f32_e32 v164, v164
	v_exp_f32_e32 v165, v165
	v_exp_f32_e32 v168, v168
	v_exp_f32_e32 v169, v169
	v_pk_fma_f32 v[142:143], v[142:143], v[144:145], v[94:95] op_sel_hi:[1,0,1]
	v_pk_fma_f32 v[138:139], v[138:139], v[144:145], v[82:83] op_sel_hi:[1,0,1]
	v_min_f32_e32 v142, 0x40e00000, v142
	v_min_f32_e32 v143, 0x40e00000, v143
	v_min_f32_e32 v138, 0x40e00000, v138
	v_min_f32_e32 v139, 0x40e00000, v139
	v_pk_mul_f32 v[166:167], v[142:143], s[36:37] op_sel_hi:[1,0]
	v_pk_mul_f32 v[170:171], v[138:139], s[36:37] op_sel_hi:[1,0]
	v_exp_f32_e32 v166, v166
	v_exp_f32_e32 v167, v167
	v_exp_f32_e32 v170, v170
	v_exp_f32_e32 v171, v171
	v_pk_add_f32 v[164:165], v[164:165], 1.0 op_sel_hi:[1,0]
	v_pk_add_f32 v[168:169], v[168:169], 1.0 op_sel_hi:[1,0]
	v_rcp_f32_e32 v164, v164
	v_rcp_f32_e32 v165, v165
	v_rcp_f32_e32 v168, v168
	v_rcp_f32_e32 v169, v169
	s_waitcnt vmcnt(0)
	v_pk_fma_f32 v[128:129], v[128:129], v[144:145], v[88:89] op_sel_hi:[1,0,1]
	v_med3_f32 v132, v132, s75, v161
	v_med3_f32 v133, v133, s75, v161
	v_med3_f32 v128, v128, s75, v161
	v_med3_f32 v129, v129, s75, v161
	v_pk_add_f32 v[166:167], v[166:167], 1.0 op_sel_hi:[1,0]
	v_pk_add_f32 v[170:171], v[170:171], 1.0 op_sel_hi:[1,0]
	v_pk_fma_f32 v[132:133], v[132:133], 4.0, 4.0 op_sel_hi:[1,0,0]
	v_pk_fma_f32 v[128:129], v[128:129], 4.0, 4.0 op_sel_hi:[1,0,0]
	v_rcp_f32_e32 v166, v166
	v_rcp_f32_e32 v167, v167
	v_rcp_f32_e32 v170, v170
	v_rcp_f32_e32 v171, v171
	v_pk_mul_f32 v[140:141], v[140:141], v[164:165]
	v_pk_mul_f32 v[136:137], v[136:137], v[168:169]
	v_pk_mul_f32 v[132:133], v[132:133], v[140:141]
	v_pk_mul_f32 v[128:129], v[128:129], v[136:137]
	v_pk_fma_f32 v[134:135], v[134:135], v[144:145], v[86:87] op_sel_hi:[1,0,1]
	v_pk_fma_f32 v[130:131], v[130:131], v[144:145], v[90:91] op_sel_hi:[1,0,1]
	v_cvt_pk_fp8_f32 v162, v132, v133
	v_cvt_pk_fp8_f32 v163, v128, v129
	v_med3_f32 v134, v134, s75, v161
	v_med3_f32 v135, v135, s75, v161
	v_med3_f32 v130, v130, s75, v161
	v_med3_f32 v131, v131, s75, v161
	v_pk_fma_f32 v[134:135], v[134:135], 4.0, 4.0 op_sel_hi:[1,0,0]
	v_pk_fma_f32 v[130:131], v[130:131], 4.0, 4.0 op_sel_hi:[1,0,0]
	v_pk_mul_f32 v[142:143], v[142:143], v[166:167]
	v_pk_mul_f32 v[138:139], v[138:139], v[170:171]
	v_pk_mul_f32 v[128:129], v[134:135], v[142:143]
	v_pk_mul_f32 v[130:131], v[130:131], v[138:139]
	v_cvt_pk_fp8_f32 v162, v128, v129 op_sel:[0,0,1]
	v_cvt_pk_fp8_f32 v163, v130, v131 op_sel:[0,0,1]
	v_subrev_co_u32_e32 v128, vcc, s35, v150
	v_mov_b32_e32 v130, v145
	s_nop 0
	v_subb_co_u32_e32 v129, vcc, v151, v172, vcc
	global_store_dwordx2 v[146:147], v[162:163], off
	v_lshl_add_u64 v[128:129], v[128:129], 2, s[48:49]
	v_mov_b32_e32 v134, v240
	v_mov_b32_e32 v131, v145
	v_or_b32_e32 v132, 16, v150
	v_ashrrev_i32_e32 v133, 31, v132
	s_mov_b32 s35, 0x40000
	v_mov_b32_e32 v144, v145
	v_mul_f32_e32 v134, 0x3c800000, v134
	v_pk_fma_f32 v[124:125], v[124:125], v[134:135], v[92:93] op_sel_hi:[1,0,1]
	v_pk_fma_f32 v[120:121], v[120:121], v[134:135], v[80:81] op_sel_hi:[1,0,1]
	v_min_f32_e32 v124, 0x40e00000, v124
	v_min_f32_e32 v125, 0x40e00000, v125
	v_min_f32_e32 v120, 0x40e00000, v120
	v_min_f32_e32 v121, 0x40e00000, v121
	v_pk_fma_f32 v[116:117], v[116:117], v[134:135], v[84:85] op_sel_hi:[1,0,1]
; __device__ __forceinline__ unsigned cvt_pk4_fp8(float a, float b, float c, float d) { int w; asm("" : "=v"(w));     w = __builtin_amdgcn_cvt_pk_fp8_f32(a, b, w, false); w = __builtin_amdgcn_cvt_pk_fp8_f32(c, d, w, true); return (unsigned)w; }
;     __device__ __forceinline__ void operator()(const f32x4 (&acc)[2][2][4][2], const Unit& u, int wr, int wc, int fr, int fq) const {
;     ...
;             for (int m = 0; m < 4; ++m) { const int r = row0 + ai * HALF + m * 16; unsigned char* rowp = O + (size_t)r * DFF + j0; const float sc = inv * rs[(size_t)u.e * XCAP + u.lr0 + (r - u.pm * BM)];
;                 float a[8];
; #pragma unroll
;                 for (int n = 0; n < 2; ++n)
; #pragma unroll
;                     for (int h = 0; h < 2; ++h) {
;                         const f32x2 ag = {acc[ai][0][m][n][2 * h], acc[ai][0][m][n][2 * h + 1]}, au = {acc[ai][1][m][n][2 * h], acc[ai][1][m][n][2 * h + 1]};
;                         const f32x2 bg2 = {bgv[n][2 * h], bgv[n][2 * h + 1]}, bu2 = {buv[n][2 * h], buv[n][2 * h + 1]};
;                         f32x2 g = ag * sc + bg2, up = au * sc + bu2;
;                         g.x = fminf(g.x, 7.0f); g.y = fminf(g.y, 7.0f);
;                         up.x = __builtin_amdgcn_fmed3f(up.x, -7.0f, 7.0f); up.y = __builtin_amdgcn_fmed3f(up.y, -7.0f, 7.0f);
;                         const f32x2 t = g * (-1.702f * 1.4426950408889634f);
;                         f32x2 e; e.x = __builtin_amdgcn_exp2f(t.x); e.y = __builtin_amdgcn_exp2f(t.y);
;                         const f32x2 d = e + 1.0f;
;                         f32x2 rr; rr.x = __builtin_amdgcn_rcpf(d.x); rr.y = __builtin_amdgcn_rcpf(d.y);
;                         const f32x2 o2 = (up * ACT8_SCALE + ACT8_SCALE) * (g * rr);
;                         a[4 * n + 2 * h] = o2.x; a[4 * n + 2 * h + 1] = o2.y; }
;                 u32x2 w; w.x = cvt_pk4_fp8(a[0], a[1], a[2], a[3]); w.y = cvt_pk4_fp8(a[4], a[5], a[6], a[7]);
;                 *(u32x2*)rowp = w; }
	v_pk_fma_f32 v[126:127], v[126:127], v[134:135], v[94:95] op_sel_hi:[1,0,1]
	v_pk_fma_f32 v[118:119], v[118:119], v[134:135], v[86:87] op_sel_hi:[1,0,1]
	v_pk_fma_f32 v[112:113], v[112:113], v[134:135], v[88:89] op_sel_hi:[1,0,1]
	v_pk_fma_f32 v[122:123], v[122:123], v[134:135], v[82:83] op_sel_hi:[1,0,1]
	v_pk_fma_f32 v[114:115], v[114:115], v[134:135], v[90:91] op_sel_hi:[1,0,1]
	v_pk_mul_f32 v[134:135], v[124:125], s[36:37] op_sel_hi:[1,0]
	v_pk_mul_f32 v[138:139], v[120:121], s[36:37] op_sel_hi:[1,0]
	v_exp_f32_e32 v134, v134
	v_exp_f32_e32 v135, v135
	v_exp_f32_e32 v138, v138
	v_exp_f32_e32 v139, v139
	v_min_f32_e32 v126, 0x40e00000, v126
	v_min_f32_e32 v127, 0x40e00000, v127
	v_min_f32_e32 v122, 0x40e00000, v122
	v_min_f32_e32 v123, 0x40e00000, v123
	v_pk_mul_f32 v[136:137], v[126:127], s[36:37] op_sel_hi:[1,0]
	v_pk_mul_f32 v[140:141], v[122:123], s[36:37] op_sel_hi:[1,0]
	v_exp_f32_e32 v136, v136
	v_exp_f32_e32 v137, v137
	v_exp_f32_e32 v140, v140
	v_exp_f32_e32 v141, v141
	v_pk_add_f32 v[134:135], v[134:135], 1.0 op_sel_hi:[1,0]
	v_pk_add_f32 v[138:139], v[138:139], 1.0 op_sel_hi:[1,0]
	v_rcp_f32_e32 v134, v134
	v_rcp_f32_e32 v135, v135
	v_rcp_f32_e32 v138, v138
	v_rcp_f32_e32 v139, v139
	v_med3_f32 v116, v116, s75, v161
	v_med3_f32 v117, v117, s75, v161
	v_med3_f32 v112, v112, s75, v161
	v_med3_f32 v113, v113, s75, v161
	v_pk_add_f32 v[136:137], v[136:137], 1.0 op_sel_hi:[1,0]
	v_pk_add_f32 v[140:141], v[140:141], 1.0 op_sel_hi:[1,0]
	v_pk_fma_f32 v[116:117], v[116:117], 4.0, 4.0 op_sel_hi:[1,0,0]
	v_pk_fma_f32 v[112:113], v[112:113], 4.0, 4.0 op_sel_hi:[1,0,0]
	v_rcp_f32_e32 v136, v136
	v_rcp_f32_e32 v137, v137
	v_rcp_f32_e32 v140, v140
	v_rcp_f32_e32 v141, v141
	v_pk_mul_f32 v[124:125], v[124:125], v[134:135]
	v_pk_mul_f32 v[120:121], v[120:121], v[138:139]
	v_pk_mul_f32 v[116:117], v[116:117], v[124:125]
	v_pk_mul_f32 v[112:113], v[112:113], v[120:121]
	v_cvt_pk_fp8_f32 v130, v116, v117
	v_cvt_pk_fp8_f32 v131, v112, v113
	v_med3_f32 v118, v118, s75, v161
	v_med3_f32 v119, v119, s75, v161
	v_med3_f32 v114, v114, s75, v161
	v_med3_f32 v115, v115, s75, v161
	v_pk_fma_f32 v[118:119], v[118:119], 4.0, 4.0 op_sel_hi:[1,0,0]
	v_pk_fma_f32 v[114:115], v[114:115], 4.0, 4.0 op_sel_hi:[1,0,0]
	v_pk_mul_f32 v[126:127], v[126:127], v[136:137]
	v_pk_mul_f32 v[122:123], v[122:123], v[140:141]
	v_pk_mul_f32 v[112:113], v[118:119], v[126:127]
	v_pk_mul_f32 v[114:115], v[114:115], v[122:123]
	v_cvt_pk_fp8_f32 v130, v112, v113 op_sel:[0,0,1]
	v_cvt_pk_fp8_f32 v131, v114, v115 op_sel:[0,0,1]
	v_lshlrev_b64 v[112:113], 11, v[132:133]
	v_lshl_add_u64 v[112:113], s[4:5], 0, v[112:113]
	v_lshl_add_u64 v[112:113], v[112:113], 0, v[148:149]
	global_store_dwordx2 v[112:113], v[130:131], off
	v_mov_b32_e32 v116, v241
	v_mov_b32_e32 v112, v145
	v_mov_b32_e32 v113, v145
	v_or_b32_e32 v114, 32, v150
	v_ashrrev_i32_e32 v115, 31, v114
	v_mul_f32_e32 v116, 0x3c800000, v116
	v_pk_fma_f32 v[108:109], v[108:109], v[116:117], v[92:93] op_sel_hi:[1,0,1]
	v_pk_fma_f32 v[104:105], v[104:105], v[116:117], v[80:81] op_sel_hi:[1,0,1]
	v_min_f32_e32 v108, 0x40e00000, v108
	v_min_f32_e32 v109, 0x40e00000, v109
	v_min_f32_e32 v104, 0x40e00000, v104
	v_min_f32_e32 v105, 0x40e00000, v105
	v_pk_fma_f32 v[100:101], v[100:101], v[116:117], v[84:85] op_sel_hi:[1,0,1]
	v_pk_fma_f32 v[110:111], v[110:111], v[116:117], v[94:95] op_sel_hi:[1,0,1]
	v_pk_fma_f32 v[102:103], v[102:103], v[116:117], v[86:87] op_sel_hi:[1,0,1]
	v_pk_fma_f32 v[96:97], v[96:97], v[116:117], v[88:89] op_sel_hi:[1,0,1]
	v_pk_fma_f32 v[106:107], v[106:107], v[116:117], v[82:83] op_sel_hi:[1,0,1]
	v_pk_fma_f32 v[98:99], v[98:99], v[116:117], v[90:91] op_sel_hi:[1,0,1]
	v_pk_mul_f32 v[116:117], v[108:109], s[36:37] op_sel_hi:[1,0]
	v_pk_mul_f32 v[120:121], v[104:105], s[36:37] op_sel_hi:[1,0]
	v_exp_f32_e32 v116, v116
	v_exp_f32_e32 v117, v117
	v_exp_f32_e32 v120, v120
	v_exp_f32_e32 v121, v121
	v_min_f32_e32 v110, 0x40e00000, v110
	v_min_f32_e32 v111, 0x40e00000, v111
	v_min_f32_e32 v106, 0x40e00000, v106
	v_min_f32_e32 v107, 0x40e00000, v107
	v_pk_mul_f32 v[118:119], v[110:111], s[36:37] op_sel_hi:[1,0]
	v_pk_mul_f32 v[122:123], v[106:107], s[36:37] op_sel_hi:[1,0]
	v_exp_f32_e32 v118, v118
	v_exp_f32_e32 v119, v119
	v_exp_f32_e32 v122, v122
	v_exp_f32_e32 v123, v123
	v_pk_add_f32 v[116:117], v[116:117], 1.0 op_sel_hi:[1,0]
	v_pk_add_f32 v[120:121], v[120:121], 1.0 op_sel_hi:[1,0]
	v_rcp_f32_e32 v116, v116
	v_rcp_f32_e32 v117, v117
	v_rcp_f32_e32 v120, v120
	v_rcp_f32_e32 v121, v121
	v_med3_f32 v100, v100, s75, v161
	v_med3_f32 v101, v101, s75, v161
	v_med3_f32 v96, v96, s75, v161
	v_med3_f32 v97, v97, s75, v161
	v_pk_add_f32 v[118:119], v[118:119], 1.0 op_sel_hi:[1,0]
	v_pk_add_f32 v[122:123], v[122:123], 1.0 op_sel_hi:[1,0]
	v_pk_fma_f32 v[100:101], v[100:101], 4.0, 4.0 op_sel_hi:[1,0,0]
	v_pk_fma_f32 v[96:97], v[96:97], 4.0, 4.0 op_sel_hi:[1,0,0]
	v_rcp_f32_e32 v118, v118
	v_rcp_f32_e32 v119, v119
	v_rcp_f32_e32 v122, v122
	v_rcp_f32_e32 v123, v123
	v_pk_mul_f32 v[108:109], v[108:109], v[116:117]
	v_pk_mul_f32 v[104:105], v[104:105], v[120:121]
	v_pk_mul_f32 v[100:101], v[100:101], v[108:109]
	v_pk_mul_f32 v[96:97], v[96:97], v[104:105]
	v_cvt_pk_fp8_f32 v112, v100, v101
	v_cvt_pk_fp8_f32 v113, v96, v97
	v_med3_f32 v102, v102, s75, v161
	v_med3_f32 v103, v103, s75, v161
	v_med3_f32 v98, v98, s75, v161
	v_med3_f32 v99, v99, s75, v161
	v_pk_fma_f32 v[102:103], v[102:103], 4.0, 4.0 op_sel_hi:[1,0,0]
	v_pk_fma_f32 v[98:99], v[98:99], 4.0, 4.0 op_sel_hi:[1,0,0]
	v_pk_mul_f32 v[110:111], v[110:111], v[118:119]
	v_pk_mul_f32 v[106:107], v[106:107], v[122:123]
	v_pk_mul_f32 v[96:97], v[102:103], v[110:111]
; __device__ __forceinline__ unsigned cvt_pk4_fp8(float a, float b, float c, float d) { int w; asm("" : "=v"(w));     w = __builtin_amdgcn_cvt_pk_fp8_f32(a, b, w, false); w = __builtin_amdgcn_cvt_pk_fp8_f32(c, d, w, true); return (unsigned)w; }
;     __device__ __forceinline__ void operator()(const f32x4 (&acc)[2][2][4][2], const Unit& u, int wr, int wc, int fr, int fq) const {
;     ...
;             for (int m = 0; m < 4; ++m) { const int r = row0 + ai * HALF + m * 16; unsigned char* rowp = O + (size_t)r * DFF + j0; const float sc = inv * rs[(size_t)u.e * XCAP + u.lr0 + (r - u.pm * BM)];
;                 float a[8];
; #pragma unroll
;                 for (int n = 0; n < 2; ++n)
; #pragma unroll
;                     for (int h = 0; h < 2; ++h) {
;                         const f32x2 ag = {acc[ai][0][m][n][2 * h], acc[ai][0][m][n][2 * h + 1]}, au = {acc[ai][1][m][n][2 * h], acc[ai][1][m][n][2 * h + 1]};
;                         const f32x2 bg2 = {bgv[n][2 * h], bgv[n][2 * h + 1]}, bu2 = {buv[n][2 * h], buv[n][2 * h + 1]};
;                         f32x2 g = ag * sc + bg2, up = au * sc + bu2;
;                         g.x = fminf(g.x, 7.0f); g.y = fminf(g.y, 7.0f);
;                         up.x = __builtin_amdgcn_fmed3f(up.x, -7.0f, 7.0f); up.y = __builtin_amdgcn_fmed3f(up.y, -7.0f, 7.0f);
;                         const f32x2 t = g * (-1.702f * 1.4426950408889634f);
;                         f32x2 e; e.x = __builtin_amdgcn_exp2f(t.x); e.y = __builtin_amdgcn_exp2f(t.y);
;                         const f32x2 d = e + 1.0f;
;                         f32x2 rr; rr.x = __builtin_amdgcn_rcpf(d.x); rr.y = __builtin_amdgcn_rcpf(d.y);
;                         const f32x2 o2 = (up * ACT8_SCALE + ACT8_SCALE) * (g * rr);
;                         a[4 * n + 2 * h] = o2.x; a[4 * n + 2 * h + 1] = o2.y; }
;                 u32x2 w; w.x = cvt_pk4_fp8(a[0], a[1], a[2], a[3]); w.y = cvt_pk4_fp8(a[4], a[5], a[6], a[7]);
;                 *(u32x2*)rowp = w; }
	v_pk_mul_f32 v[98:99], v[98:99], v[106:107]
	v_cvt_pk_fp8_f32 v112, v96, v97 op_sel:[0,0,1]
	v_cvt_pk_fp8_f32 v113, v98, v99 op_sel:[0,0,1]
	v_lshlrev_b64 v[96:97], 11, v[114:115]
	v_lshl_add_u64 v[96:97], s[4:5], 0, v[96:97]
	v_lshl_add_u64 v[96:97], v[96:97], 0, v[148:149]
	global_store_dwordx2 v[96:97], v[112:113], off
	v_mov_b32_e32 v100, v242
	v_mov_b32_e32 v96, v145
	v_mov_b32_e32 v97, v145
	v_or_b32_e32 v98, 48, v150
	v_ashrrev_i32_e32 v99, 31, v98
	v_mul_f32_e32 v100, 0x3c800000, v100
	v_pk_fma_f32 v[76:77], v[76:77], v[100:101], v[92:93] op_sel_hi:[1,0,1]
	v_pk_fma_f32 v[72:73], v[72:73], v[100:101], v[80:81] op_sel_hi:[1,0,1]
	v_min_f32_e32 v76, 0x40e00000, v76
	v_min_f32_e32 v77, 0x40e00000, v77
	v_min_f32_e32 v72, 0x40e00000, v72
	v_min_f32_e32 v73, 0x40e00000, v73
	v_pk_fma_f32 v[68:69], v[68:69], v[100:101], v[84:85] op_sel_hi:[1,0,1]
	v_pk_fma_f32 v[78:79], v[78:79], v[100:101], v[94:95] op_sel_hi:[1,0,1]
	v_pk_fma_f32 v[70:71], v[70:71], v[100:101], v[86:87] op_sel_hi:[1,0,1]
	v_pk_fma_f32 v[64:65], v[64:65], v[100:101], v[88:89] op_sel_hi:[1,0,1]
	v_pk_fma_f32 v[74:75], v[74:75], v[100:101], v[82:83] op_sel_hi:[1,0,1]
	v_pk_fma_f32 v[66:67], v[66:67], v[100:101], v[90:91] op_sel_hi:[1,0,1]
	v_pk_mul_f32 v[100:101], v[76:77], s[36:37] op_sel_hi:[1,0]
	v_pk_mul_f32 v[104:105], v[72:73], s[36:37] op_sel_hi:[1,0]
	v_exp_f32_e32 v100, v100
	v_exp_f32_e32 v101, v101
	v_exp_f32_e32 v104, v104
	v_exp_f32_e32 v105, v105
	v_min_f32_e32 v78, 0x40e00000, v78
	v_min_f32_e32 v79, 0x40e00000, v79
	v_min_f32_e32 v74, 0x40e00000, v74
	v_min_f32_e32 v75, 0x40e00000, v75
	v_pk_mul_f32 v[102:103], v[78:79], s[36:37] op_sel_hi:[1,0]
	v_pk_mul_f32 v[106:107], v[74:75], s[36:37] op_sel_hi:[1,0]
	v_exp_f32_e32 v102, v102
	v_exp_f32_e32 v103, v103
	v_exp_f32_e32 v106, v106
	v_exp_f32_e32 v107, v107
	v_pk_add_f32 v[100:101], v[100:101], 1.0 op_sel_hi:[1,0]
	v_pk_add_f32 v[104:105], v[104:105], 1.0 op_sel_hi:[1,0]
	v_rcp_f32_e32 v100, v100
	v_rcp_f32_e32 v101, v101
	v_rcp_f32_e32 v104, v104
	v_rcp_f32_e32 v105, v105
	v_med3_f32 v68, v68, s75, v161
	v_med3_f32 v69, v69, s75, v161
	v_med3_f32 v64, v64, s75, v161
	v_med3_f32 v65, v65, s75, v161
	v_pk_add_f32 v[102:103], v[102:103], 1.0 op_sel_hi:[1,0]
	v_pk_add_f32 v[106:107], v[106:107], 1.0 op_sel_hi:[1,0]
	v_pk_fma_f32 v[68:69], v[68:69], 4.0, 4.0 op_sel_hi:[1,0,0]
	v_pk_fma_f32 v[64:65], v[64:65], 4.0, 4.0 op_sel_hi:[1,0,0]
	v_rcp_f32_e32 v102, v102
	v_rcp_f32_e32 v103, v103
	v_rcp_f32_e32 v106, v106
	v_rcp_f32_e32 v107, v107
	v_pk_mul_f32 v[76:77], v[76:77], v[100:101]
	v_pk_mul_f32 v[72:73], v[72:73], v[104:105]
	v_pk_mul_f32 v[68:69], v[68:69], v[76:77]
	v_pk_mul_f32 v[64:65], v[64:65], v[72:73]
	v_cvt_pk_fp8_f32 v96, v68, v69
	v_cvt_pk_fp8_f32 v97, v64, v65
	v_med3_f32 v70, v70, s75, v161
	v_med3_f32 v71, v71, s75, v161
	v_med3_f32 v66, v66, s75, v161
	v_med3_f32 v67, v67, s75, v161
	v_pk_fma_f32 v[70:71], v[70:71], 4.0, 4.0 op_sel_hi:[1,0,0]
	v_pk_fma_f32 v[66:67], v[66:67], 4.0, 4.0 op_sel_hi:[1,0,0]
	v_pk_mul_f32 v[78:79], v[78:79], v[102:103]
	v_pk_mul_f32 v[74:75], v[74:75], v[106:107]
	v_pk_mul_f32 v[64:65], v[70:71], v[78:79]
	v_pk_mul_f32 v[66:67], v[66:67], v[74:75]
	v_cvt_pk_fp8_f32 v96, v64, v65 op_sel:[0,0,1]
	v_cvt_pk_fp8_f32 v97, v66, v67 op_sel:[0,0,1]
	v_lshlrev_b64 v[64:65], 11, v[98:99]
	v_lshl_add_u64 v[64:65], s[4:5], 0, v[64:65]
	v_lshl_add_u64 v[64:65], v[64:65], 0, v[148:149]
	global_store_dwordx2 v[64:65], v[96:97], off
	v_mov_b32_e32 v66, v243
	v_mov_b32_e32 v64, v145
	v_mov_b32_e32 v65, v145
	v_mul_f32_e32 v66, 0x3c800000, v66
	v_pk_fma_f32 v[60:61], v[60:61], v[66:67], v[92:93] op_sel_hi:[1,0,1]
	v_pk_fma_f32 v[56:57], v[56:57], v[66:67], v[80:81] op_sel_hi:[1,0,1]
	v_min_f32_e32 v60, 0x40e00000, v60
	v_min_f32_e32 v61, 0x40e00000, v61
	v_min_f32_e32 v56, 0x40e00000, v56
	v_min_f32_e32 v57, 0x40e00000, v57
	v_pk_fma_f32 v[52:53], v[52:53], v[66:67], v[84:85] op_sel_hi:[1,0,1]
	v_pk_fma_f32 v[62:63], v[62:63], v[66:67], v[94:95] op_sel_hi:[1,0,1]
	v_pk_fma_f32 v[54:55], v[54:55], v[66:67], v[86:87] op_sel_hi:[1,0,1]
	v_pk_fma_f32 v[48:49], v[48:49], v[66:67], v[88:89] op_sel_hi:[1,0,1]
	v_pk_fma_f32 v[58:59], v[58:59], v[66:67], v[82:83] op_sel_hi:[1,0,1]
	v_pk_fma_f32 v[50:51], v[50:51], v[66:67], v[90:91] op_sel_hi:[1,0,1]
	v_pk_mul_f32 v[66:67], v[60:61], s[36:37] op_sel_hi:[1,0]
	v_pk_mul_f32 v[70:71], v[56:57], s[36:37] op_sel_hi:[1,0]
	v_exp_f32_e32 v66, v66
	v_exp_f32_e32 v67, v67
	v_exp_f32_e32 v70, v70
	v_exp_f32_e32 v71, v71
	v_min_f32_e32 v62, 0x40e00000, v62
	v_min_f32_e32 v63, 0x40e00000, v63
	v_min_f32_e32 v58, 0x40e00000, v58
	v_min_f32_e32 v59, 0x40e00000, v59
	v_pk_mul_f32 v[68:69], v[62:63], s[36:37] op_sel_hi:[1,0]
	v_pk_mul_f32 v[72:73], v[58:59], s[36:37] op_sel_hi:[1,0]
	v_exp_f32_e32 v68, v68
	v_exp_f32_e32 v69, v69
	v_exp_f32_e32 v72, v72
	v_exp_f32_e32 v73, v73
	v_pk_add_f32 v[66:67], v[66:67], 1.0 op_sel_hi:[1,0]
	v_pk_add_f32 v[70:71], v[70:71], 1.0 op_sel_hi:[1,0]
	v_rcp_f32_e32 v66, v66
	v_rcp_f32_e32 v67, v67
	v_rcp_f32_e32 v70, v70
	v_rcp_f32_e32 v71, v71
	v_med3_f32 v52, v52, s75, v161
	v_med3_f32 v53, v53, s75, v161
	v_med3_f32 v48, v48, s75, v161
	v_med3_f32 v49, v49, s75, v161
	v_pk_add_f32 v[68:69], v[68:69], 1.0 op_sel_hi:[1,0]
	v_pk_add_f32 v[72:73], v[72:73], 1.0 op_sel_hi:[1,0]
	v_pk_fma_f32 v[52:53], v[52:53], 4.0, 4.0 op_sel_hi:[1,0,0]
	v_pk_fma_f32 v[48:49], v[48:49], 4.0, 4.0 op_sel_hi:[1,0,0]
	v_rcp_f32_e32 v68, v68
	v_rcp_f32_e32 v69, v69
	v_rcp_f32_e32 v72, v72
	v_rcp_f32_e32 v73, v73
	v_pk_mul_f32 v[60:61], v[60:61], v[66:67]
	v_pk_mul_f32 v[56:57], v[56:57], v[70:71]
	v_pk_mul_f32 v[52:53], v[52:53], v[60:61]
; __device__ __forceinline__ unsigned cvt_pk4_fp8(float a, float b, float c, float d) { int w; asm("" : "=v"(w));     w = __builtin_amdgcn_cvt_pk_fp8_f32(a, b, w, false); w = __builtin_amdgcn_cvt_pk_fp8_f32(c, d, w, true); return (unsigned)w; }
;     __device__ __forceinline__ void operator()(const f32x4 (&acc)[2][2][4][2], const Unit& u, int wr, int wc, int fr, int fq) const {
;     ...
;             for (int m = 0; m < 4; ++m) { const int r = row0 + ai * HALF + m * 16; unsigned char* rowp = O + (size_t)r * DFF + j0; const float sc = inv * rs[(size_t)u.e * XCAP + u.lr0 + (r - u.pm * BM)];
;                 float a[8];
; #pragma unroll
;                 for (int n = 0; n < 2; ++n)
; #pragma unroll
;                     for (int h = 0; h < 2; ++h) {
;                         const f32x2 ag = {acc[ai][0][m][n][2 * h], acc[ai][0][m][n][2 * h + 1]}, au = {acc[ai][1][m][n][2 * h], acc[ai][1][m][n][2 * h + 1]};
;                         const f32x2 bg2 = {bgv[n][2 * h], bgv[n][2 * h + 1]}, bu2 = {buv[n][2 * h], buv[n][2 * h + 1]};
;                         f32x2 g = ag * sc + bg2, up = au * sc + bu2;
;                         g.x = fminf(g.x, 7.0f); g.y = fminf(g.y, 7.0f);
;                         up.x = __builtin_amdgcn_fmed3f(up.x, -7.0f, 7.0f); up.y = __builtin_amdgcn_fmed3f(up.y, -7.0f, 7.0f);
;                         const f32x2 t = g * (-1.702f * 1.4426950408889634f);
;                         f32x2 e; e.x = __builtin_amdgcn_exp2f(t.x); e.y = __builtin_amdgcn_exp2f(t.y);
;                         const f32x2 d = e + 1.0f;
;                         f32x2 rr; rr.x = __builtin_amdgcn_rcpf(d.x); rr.y = __builtin_amdgcn_rcpf(d.y);
;                         const f32x2 o2 = (up * ACT8_SCALE + ACT8_SCALE) * (g * rr);
;                         a[4 * n + 2 * h] = o2.x; a[4 * n + 2 * h + 1] = o2.y; }
;                 u32x2 w; w.x = cvt_pk4_fp8(a[0], a[1], a[2], a[3]); w.y = cvt_pk4_fp8(a[4], a[5], a[6], a[7]);
;                 *(u32x2*)rowp = w; }
	v_pk_mul_f32 v[48:49], v[48:49], v[56:57]
	v_cvt_pk_fp8_f32 v64, v52, v53
	v_cvt_pk_fp8_f32 v65, v48, v49
	v_med3_f32 v54, v54, s75, v161
	v_med3_f32 v55, v55, s75, v161
	v_med3_f32 v50, v50, s75, v161
	v_med3_f32 v51, v51, s75, v161
	v_pk_fma_f32 v[54:55], v[54:55], 4.0, 4.0 op_sel_hi:[1,0,0]
	v_pk_fma_f32 v[50:51], v[50:51], 4.0, 4.0 op_sel_hi:[1,0,0]
	v_pk_mul_f32 v[62:63], v[62:63], v[68:69]
	v_pk_mul_f32 v[58:59], v[58:59], v[72:73]
	v_pk_mul_f32 v[48:49], v[54:55], v[62:63]
	v_pk_mul_f32 v[50:51], v[50:51], v[58:59]
	v_cvt_pk_fp8_f32 v64, v48, v49 op_sel:[0,0,1]
	v_cvt_pk_fp8_f32 v65, v50, v51 op_sel:[0,0,1]
	v_add_co_u32_e32 v48, vcc, s35, v146
	s_nop 1
	v_addc_co_u32_e32 v49, vcc, 0, v147, vcc
	global_store_dwordx2 v[48:49], v[64:65], off
	v_mov_b32_e32 v50, v244
	v_mov_b32_e32 v48, v145
	v_mov_b32_e32 v49, v145
	v_mul_f32_e32 v50, 0x3c800000, v50
	v_pk_fma_f32 v[44:45], v[44:45], v[50:51], v[92:93] op_sel_hi:[1,0,1]
	v_pk_fma_f32 v[40:41], v[40:41], v[50:51], v[80:81] op_sel_hi:[1,0,1]
	v_min_f32_e32 v44, 0x40e00000, v44
	v_min_f32_e32 v45, 0x40e00000, v45
	v_min_f32_e32 v40, 0x40e00000, v40
	v_min_f32_e32 v41, 0x40e00000, v41
	v_pk_fma_f32 v[36:37], v[36:37], v[50:51], v[84:85] op_sel_hi:[1,0,1]
	v_pk_fma_f32 v[46:47], v[46:47], v[50:51], v[94:95] op_sel_hi:[1,0,1]
	v_pk_fma_f32 v[38:39], v[38:39], v[50:51], v[86:87] op_sel_hi:[1,0,1]
	v_pk_fma_f32 v[32:33], v[32:33], v[50:51], v[88:89] op_sel_hi:[1,0,1]
	v_pk_fma_f32 v[42:43], v[42:43], v[50:51], v[82:83] op_sel_hi:[1,0,1]
	v_pk_fma_f32 v[34:35], v[34:35], v[50:51], v[90:91] op_sel_hi:[1,0,1]
	v_pk_mul_f32 v[50:51], v[44:45], s[36:37] op_sel_hi:[1,0]
	v_pk_mul_f32 v[54:55], v[40:41], s[36:37] op_sel_hi:[1,0]
	v_exp_f32_e32 v50, v50
	v_exp_f32_e32 v51, v51
	v_exp_f32_e32 v54, v54
	v_exp_f32_e32 v55, v55
	v_min_f32_e32 v46, 0x40e00000, v46
	v_min_f32_e32 v47, 0x40e00000, v47
	v_min_f32_e32 v42, 0x40e00000, v42
	v_min_f32_e32 v43, 0x40e00000, v43
	v_pk_mul_f32 v[52:53], v[46:47], s[36:37] op_sel_hi:[1,0]
	v_pk_mul_f32 v[56:57], v[42:43], s[36:37] op_sel_hi:[1,0]
	v_exp_f32_e32 v52, v52
	v_exp_f32_e32 v53, v53
	v_exp_f32_e32 v56, v56
	v_exp_f32_e32 v57, v57
	v_pk_add_f32 v[50:51], v[50:51], 1.0 op_sel_hi:[1,0]
	v_pk_add_f32 v[54:55], v[54:55], 1.0 op_sel_hi:[1,0]
	v_rcp_f32_e32 v50, v50
	v_rcp_f32_e32 v51, v51
	v_rcp_f32_e32 v54, v54
	v_rcp_f32_e32 v55, v55
	v_med3_f32 v36, v36, s75, v161
	v_med3_f32 v37, v37, s75, v161
	v_med3_f32 v32, v32, s75, v161
	v_med3_f32 v33, v33, s75, v161
	v_pk_add_f32 v[52:53], v[52:53], 1.0 op_sel_hi:[1,0]
	v_pk_add_f32 v[56:57], v[56:57], 1.0 op_sel_hi:[1,0]
	v_pk_fma_f32 v[36:37], v[36:37], 4.0, 4.0 op_sel_hi:[1,0,0]
	v_pk_fma_f32 v[32:33], v[32:33], 4.0, 4.0 op_sel_hi:[1,0,0]
	v_rcp_f32_e32 v52, v52
	v_rcp_f32_e32 v53, v53
	v_rcp_f32_e32 v56, v56
	v_rcp_f32_e32 v57, v57
	v_pk_mul_f32 v[44:45], v[44:45], v[50:51]
	v_pk_mul_f32 v[40:41], v[40:41], v[54:55]
	v_pk_mul_f32 v[36:37], v[36:37], v[44:45]
	v_pk_mul_f32 v[32:33], v[32:33], v[40:41]
	v_cvt_pk_fp8_f32 v48, v36, v37
	v_cvt_pk_fp8_f32 v49, v32, v33
	v_med3_f32 v38, v38, s75, v161
	v_med3_f32 v39, v39, s75, v161
	v_med3_f32 v34, v34, s75, v161
	v_med3_f32 v35, v35, s75, v161
	v_pk_fma_f32 v[38:39], v[38:39], 4.0, 4.0 op_sel_hi:[1,0,0]
	v_pk_fma_f32 v[34:35], v[34:35], 4.0, 4.0 op_sel_hi:[1,0,0]
	v_pk_mul_f32 v[46:47], v[46:47], v[52:53]
	v_pk_mul_f32 v[42:43], v[42:43], v[56:57]
	v_pk_mul_f32 v[32:33], v[38:39], v[46:47]
	v_pk_mul_f32 v[34:35], v[34:35], v[42:43]
	v_cvt_pk_fp8_f32 v48, v32, v33 op_sel:[0,0,1]
	v_cvt_pk_fp8_f32 v49, v34, v35 op_sel:[0,0,1]
	v_add_co_u32_e32 v32, vcc, s76, v146
	s_nop 1
	v_addc_co_u32_e32 v33, vcc, 0, v147, vcc
	global_store_dwordx2 v[32:33], v[48:49], off
	v_mov_b32_e32 v34, v245
	v_mov_b32_e32 v32, v145
	v_mov_b32_e32 v33, v145
	v_mul_f32_e32 v34, 0x3c800000, v34
	v_pk_fma_f32 v[28:29], v[28:29], v[34:35], v[92:93] op_sel_hi:[1,0,1]
	v_pk_fma_f32 v[24:25], v[24:25], v[34:35], v[80:81] op_sel_hi:[1,0,1]
	v_min_f32_e32 v28, 0x40e00000, v28
	v_min_f32_e32 v29, 0x40e00000, v29
	v_min_f32_e32 v24, 0x40e00000, v24
	v_min_f32_e32 v25, 0x40e00000, v25
	v_pk_fma_f32 v[20:21], v[20:21], v[34:35], v[84:85] op_sel_hi:[1,0,1]
	v_pk_fma_f32 v[30:31], v[30:31], v[34:35], v[94:95] op_sel_hi:[1,0,1]
	v_pk_fma_f32 v[22:23], v[22:23], v[34:35], v[86:87] op_sel_hi:[1,0,1]
	v_pk_fma_f32 v[16:17], v[16:17], v[34:35], v[88:89] op_sel_hi:[1,0,1]
	v_pk_fma_f32 v[26:27], v[26:27], v[34:35], v[82:83] op_sel_hi:[1,0,1]
	v_pk_fma_f32 v[18:19], v[18:19], v[34:35], v[90:91] op_sel_hi:[1,0,1]
	v_pk_mul_f32 v[34:35], v[28:29], s[36:37] op_sel_hi:[1,0]
	v_pk_mul_f32 v[38:39], v[24:25], s[36:37] op_sel_hi:[1,0]
	v_exp_f32_e32 v34, v34
	v_exp_f32_e32 v35, v35
	v_exp_f32_e32 v38, v38
	v_exp_f32_e32 v39, v39
	v_min_f32_e32 v30, 0x40e00000, v30
	v_min_f32_e32 v31, 0x40e00000, v31
; #define PG8_BAR __builtin_amdgcn_s_barrier()
;     __device__ __forceinline__ void operator()(const f32x4 (&acc)[2][2][4][2], const Unit& u, int wr, int wc, int fr, int fq) const {
;     ...
;             for (int m = 0; m < 4; ++m) { const int r = row0 + ai * HALF + m * 16; unsigned char* rowp = O + (size_t)r * DFF + j0; const float sc = inv * rs[(size_t)u.e * XCAP + u.lr0 + (r - u.pm * BM)];
;                 float a[8];
; #pragma unroll
;                 for (int n = 0; n < 2; ++n)
; #pragma unroll
;                     for (int h = 0; h < 2; ++h) {
;                         const f32x2 ag = {acc[ai][0][m][n][2 * h], acc[ai][0][m][n][2 * h + 1]}, au = {acc[ai][1][m][n][2 * h], acc[ai][1][m][n][2 * h + 1]};
;                         const f32x2 bg2 = {bgv[n][2 * h], bgv[n][2 * h + 1]}, bu2 = {buv[n][2 * h], buv[n][2 * h + 1]};
;                         f32x2 g = ag * sc + bg2, up = au * sc + bu2;
;                         g.x = fminf(g.x, 7.0f); g.y = fminf(g.y, 7.0f);
;                         up.x = __builtin_amdgcn_fmed3f(up.x, -7.0f, 7.0f); up.y = __builtin_amdgcn_fmed3f(up.y, -7.0f, 7.0f);
;                         const f32x2 t = g * (-1.702f * 1.4426950408889634f);
;                         f32x2 e; e.x = __builtin_amdgcn_exp2f(t.x); e.y = __builtin_amdgcn_exp2f(t.y);
;                         const f32x2 d = e + 1.0f;
;                         f32x2 rr; rr.x = __builtin_amdgcn_rcpf(d.x); rr.y = __builtin_amdgcn_rcpf(d.y);
;                         const f32x2 o2 = (up * ACT8_SCALE + ACT8_SCALE) * (g * rr);
;                         a[4 * n + 2 * h] = o2.x; a[4 * n + 2 * h + 1] = o2.y; }
;                 u32x2 w; w.x = cvt_pk4_fp8(a[0], a[1], a[2], a[3]); w.y = cvt_pk4_fp8(a[4], a[5], a[6], a[7]);
;                 *(u32x2*)rowp = w; }
; template <bool FP8 = false, class Epi, class Sched>
; __device__ __forceinline__ void gemm_phase(LAS unsigned char* lds, const int K, const int lda, const int ldb, const Sched& S, const Epi& E, const int wid) {
;     ...
;         if (!has_next) break;
; #pragma unroll
;         for (int a = 0; a < 2; ++a)
; #pragma unroll
;             for (int b = 0; b < 2; ++b)
; #pragma unroll
;                 for (int m = 0; m < 4; ++m)
; #pragma unroll
;                     for (int n = 0; n < 2; ++n) acc[a][b][m][n] = (f32x4){0.f, 0.f, 0.f, 0.f};
;         cur = nxt; cA = nA; cB = nB; ++ui;
;         if (wr == 1) PG8_BAR;
	v_min_f32_e32 v26, 0x40e00000, v26
	v_min_f32_e32 v27, 0x40e00000, v27
	v_pk_mul_f32 v[36:37], v[30:31], s[36:37] op_sel_hi:[1,0]
	v_pk_mul_f32 v[40:41], v[26:27], s[36:37] op_sel_hi:[1,0]
	v_exp_f32_e32 v36, v36
	v_exp_f32_e32 v37, v37
	v_exp_f32_e32 v40, v40
	v_exp_f32_e32 v41, v41
	v_pk_add_f32 v[34:35], v[34:35], 1.0 op_sel_hi:[1,0]
	v_pk_add_f32 v[38:39], v[38:39], 1.0 op_sel_hi:[1,0]
	v_rcp_f32_e32 v34, v34
	v_rcp_f32_e32 v35, v35
	v_rcp_f32_e32 v38, v38
	v_rcp_f32_e32 v39, v39
	v_med3_f32 v20, v20, s75, v161
	v_med3_f32 v21, v21, s75, v161
	v_med3_f32 v16, v16, s75, v161
	v_med3_f32 v17, v17, s75, v161
	v_pk_add_f32 v[36:37], v[36:37], 1.0 op_sel_hi:[1,0]
	v_pk_add_f32 v[40:41], v[40:41], 1.0 op_sel_hi:[1,0]
	v_pk_fma_f32 v[20:21], v[20:21], 4.0, 4.0 op_sel_hi:[1,0,0]
	v_pk_fma_f32 v[16:17], v[16:17], 4.0, 4.0 op_sel_hi:[1,0,0]
	v_rcp_f32_e32 v36, v36
	v_rcp_f32_e32 v37, v37
	v_rcp_f32_e32 v40, v40
	v_rcp_f32_e32 v41, v41
	v_pk_mul_f32 v[28:29], v[28:29], v[34:35]
	v_pk_mul_f32 v[24:25], v[24:25], v[38:39]
	v_pk_mul_f32 v[20:21], v[20:21], v[28:29]
	v_pk_mul_f32 v[16:17], v[16:17], v[24:25]
	v_cvt_pk_fp8_f32 v32, v20, v21
	v_cvt_pk_fp8_f32 v33, v16, v17
	v_med3_f32 v22, v22, s75, v161
	v_med3_f32 v23, v23, s75, v161
	v_med3_f32 v18, v18, s75, v161
	v_med3_f32 v19, v19, s75, v161
	v_pk_fma_f32 v[22:23], v[22:23], 4.0, 4.0 op_sel_hi:[1,0,0]
	v_pk_fma_f32 v[18:19], v[18:19], 4.0, 4.0 op_sel_hi:[1,0,0]
	v_pk_mul_f32 v[30:31], v[30:31], v[36:37]
	v_pk_mul_f32 v[26:27], v[26:27], v[40:41]
	v_pk_mul_f32 v[16:17], v[22:23], v[30:31]
	v_pk_mul_f32 v[18:19], v[18:19], v[26:27]
	v_cvt_pk_fp8_f32 v32, v16, v17 op_sel:[0,0,1]
	v_cvt_pk_fp8_f32 v33, v18, v19 op_sel:[0,0,1]
	v_add_co_u32_e32 v16, vcc, s77, v146
	s_nop 1
	v_addc_co_u32_e32 v17, vcc, 0, v147, vcc
	global_store_dwordx2 v[16:17], v[32:33], off
	v_mov_b32_e32 v17, v246
	v_add_co_u32_e32 v16, vcc, 0x58000, v146
	v_mul_f32_e32 v18, 0x3c800000, v17
	v_pk_fma_f32 v[12:13], v[12:13], v[18:19], v[92:93] op_sel_hi:[1,0,1]
	v_pk_fma_f32 v[8:9], v[8:9], v[18:19], v[80:81] op_sel_hi:[1,0,1]
	v_min_f32_e32 v12, 0x40e00000, v12
	v_min_f32_e32 v13, 0x40e00000, v13
	v_min_f32_e32 v8, 0x40e00000, v8
	v_min_f32_e32 v9, 0x40e00000, v9
	v_pk_fma_f32 v[4:5], v[4:5], v[18:19], v[84:85] op_sel_hi:[1,0,1]
	v_pk_fma_f32 v[14:15], v[14:15], v[18:19], v[94:95] op_sel_hi:[1,0,1]
	v_pk_fma_f32 v[6:7], v[6:7], v[18:19], v[86:87] op_sel_hi:[1,0,1]
	v_pk_fma_f32 v[0:1], v[0:1], v[18:19], v[88:89] op_sel_hi:[1,0,1]
	v_pk_fma_f32 v[10:11], v[10:11], v[18:19], v[82:83] op_sel_hi:[1,0,1]
	v_pk_fma_f32 v[2:3], v[2:3], v[18:19], v[90:91] op_sel_hi:[1,0,1]
	v_pk_mul_f32 v[18:19], v[12:13], s[36:37] op_sel_hi:[1,0]
	v_pk_mul_f32 v[22:23], v[8:9], s[36:37] op_sel_hi:[1,0]
	v_exp_f32_e32 v18, v18
	v_exp_f32_e32 v19, v19
	v_exp_f32_e32 v22, v22
	v_exp_f32_e32 v23, v23
	v_min_f32_e32 v14, 0x40e00000, v14
	v_min_f32_e32 v15, 0x40e00000, v15
	v_min_f32_e32 v10, 0x40e00000, v10
	v_min_f32_e32 v11, 0x40e00000, v11
	v_pk_mul_f32 v[20:21], v[14:15], s[36:37] op_sel_hi:[1,0]
	v_pk_mul_f32 v[24:25], v[10:11], s[36:37] op_sel_hi:[1,0]
	v_exp_f32_e32 v20, v20
	v_exp_f32_e32 v21, v21
	v_exp_f32_e32 v24, v24
	v_exp_f32_e32 v25, v25
	v_pk_add_f32 v[18:19], v[18:19], 1.0 op_sel_hi:[1,0]
	v_pk_add_f32 v[22:23], v[22:23], 1.0 op_sel_hi:[1,0]
	v_rcp_f32_e32 v18, v18
	v_rcp_f32_e32 v19, v19
	v_rcp_f32_e32 v22, v22
	v_rcp_f32_e32 v23, v23
	v_med3_f32 v4, v4, s75, v161
	v_med3_f32 v5, v5, s75, v161
	v_med3_f32 v0, v0, s75, v161
	v_med3_f32 v1, v1, s75, v161
	v_pk_add_f32 v[20:21], v[20:21], 1.0 op_sel_hi:[1,0]
	v_pk_add_f32 v[24:25], v[24:25], 1.0 op_sel_hi:[1,0]
	v_pk_fma_f32 v[4:5], v[4:5], 4.0, 4.0 op_sel_hi:[1,0,0]
	v_pk_fma_f32 v[0:1], v[0:1], 4.0, 4.0 op_sel_hi:[1,0,0]
	v_rcp_f32_e32 v20, v20
	v_rcp_f32_e32 v21, v21
	v_rcp_f32_e32 v24, v24
	v_rcp_f32_e32 v25, v25
	v_pk_mul_f32 v[12:13], v[12:13], v[18:19]
	v_pk_mul_f32 v[8:9], v[8:9], v[22:23]
	v_pk_mul_f32 v[4:5], v[4:5], v[12:13]
	v_pk_mul_f32 v[0:1], v[0:1], v[8:9]
	v_cvt_pk_fp8_f32 v144, v4, v5
	v_cvt_pk_fp8_f32 v145, v0, v1
	v_med3_f32 v6, v6, s75, v161
	v_med3_f32 v7, v7, s75, v161
	v_med3_f32 v2, v2, s75, v161
	v_med3_f32 v3, v3, s75, v161
	v_pk_fma_f32 v[6:7], v[6:7], 4.0, 4.0 op_sel_hi:[1,0,0]
	v_pk_fma_f32 v[2:3], v[2:3], 4.0, 4.0 op_sel_hi:[1,0,0]
	v_pk_mul_f32 v[14:15], v[14:15], v[20:21]
	v_pk_mul_f32 v[10:11], v[10:11], v[24:25]
	v_pk_mul_f32 v[0:1], v[6:7], v[14:15]
	v_pk_mul_f32 v[2:3], v[2:3], v[10:11]
	v_cvt_pk_fp8_f32 v144, v0, v1 op_sel:[0,0,1]
	v_cvt_pk_fp8_f32 v145, v2, v3 op_sel:[0,0,1]
	v_addc_co_u32_e32 v17, vcc, 0, v147, vcc
	s_andn2_b64 vcc, exec, s[40:41]
	s_mov_b64 s[40:41], -1
	global_store_dwordx2 v[16:17], v[144:145], off
	s_cbranch_vccnz .LBB0_1055
	s_andn2_b64 vcc, exec, s[10:11]
	s_cbranch_vccnz .LBB0_1054
	s_barrier
	s_branch .LBB0_1054

; __device__ __forceinline__ unsigned cvt_pk4_fp8(float a, float b, float c, float d) { int w; asm("" : "=v"(w));     w = __builtin_amdgcn_cvt_pk_fp8_f32(a, b, w, false); w = __builtin_amdgcn_cvt_pk_fp8_f32(c, d, w, true); return (unsigned)w; }
;     __device__ __forceinline__ void operator()(const f32x4 (&acc)[2][2][4][2], const Unit& u, int wr, int wc, int fr, int fq) const {
;         const int row0 = u.pm * BM + wr * 64 + fr, col0 = u.pn * BM + wc * 32 + 8 * fq;
;         const float* b = bd + (size_t)u.e * DM + col0;
;         f32x4 bv[2][2];
; #pragma unroll
;         for (int bj = 0; bj < 2; ++bj)
; #pragma unroll
;             for (int n = 0; n < 2; ++n) bv[bj][n] = *(const f32x4*)(b + bj * HALF + 4 * n);
; #pragma unroll
;         for (int ai = 0; ai < 2; ++ai)
; #pragma unroll
;             for (int m = 0; m < 4; ++m) { const int r = row0 + ai * HALF + m * 16; const float rw = row_w[(size_t)u.e * XCAP + u.lr0 + (r - u.pm * BM)] * Y8_SCALE; unsigned char* rowp = O + (size_t)r * DM + col0;
; #pragma unroll
;                 for (int bj = 0; bj < 2; ++bj) { const f32x4 v0 = (acc[ai][bj][m][0] * (1.0f / (W8_SCALE * ACT8_SCALE)) + bv[bj][0]) * rw, v1 = (acc[ai][bj][m][1] * (1.0f / (W8_SCALE * ACT8_SCALE)) + bv[bj][1]) * rw;
;                     u32x2 w; w.x = cvt_pk4_fp8(v0[0], v0[1], v0[2], v0[3]); w.y = cvt_pk4_fp8(v1[0], v1[1], v1[2], v1[3]);
;                     *(u32x2*)(rowp + bj * HALF) = w; } }
.LBB0_1136:
	s_lshl_b32 s49, s58, 8
	v_readlane_b32 s51, v252, 28
	s_ashr_i32 s57, s56, 31
	s_lshl_b32 s45, s60, 8
	s_or_b32 s49, s49, s51
	s_lshl_b64 s[64:65], s[56:57], 13
	v_mbcnt_lo_u32_b32 v144, -1, 0
	v_mbcnt_hi_u32_b32 v144, -1, v144
	s_add_u32 s64, s10, s64
	v_ashrrev_i32_e32 v128, 1, v144
	v_and_b32_e32 v128, -8, v128
	s_addc_u32 s65, s11, s65
	s_ashr_i32 s63, s62, 31
	s_lshl_b64 s[56:57], s[56:57], 16
	v_add_u32_e32 v148, s49, v128
	s_add_u32 s49, s22, s56
	s_addc_u32 s51, s23, s57
	s_lshl_b64 s[56:57], s[62:63], 2
	v_ashrrev_i32_e32 v149, 31, v148
	v_and_or_b32 v144, v144, 15, s34
	s_add_u32 s56, s49, s56
	v_lshl_add_u64 v[136:137], v[148:149], 2, s[64:65]
	s_addc_u32 s57, s51, s57
	v_lshlrev_b32_e32 v145, 2, v144
	global_load_dword v240, v145, s[56:57] offset:64
	global_load_dword v241, v145, s[56:57] offset:128
	global_load_dword v242, v145, s[56:57] offset:192
	global_load_dword v243, v145, s[56:57] offset:512
	global_load_dword v244, v145, s[56:57] offset:576
	global_load_dword v245, v145, s[56:57] offset:640
	global_load_dword v246, v145, s[56:57] offset:704
	global_load_dwordx4 v[132:135], v[136:137], off offset:16
	global_load_dwordx4 v[140:143], v[136:137], off
	global_load_dwordx4 v[128:131], v[136:137], off offset:528
	s_nop 0
	global_load_dwordx4 v[136:139], v[136:137], off offset:512
	v_add_u32_e32 v150, s45, v144
	global_load_dword v161, v145, s[56:57]
	v_ashrrev_i32_e32 v151, 31, v150
	v_mov_b32_e32 v162, v145
	v_mov_b32_e32 v163, v145
	v_mov_b32_e32 v164, v145
	v_mov_b32_e32 v165, v145
	v_lshlrev_b64 v[146:147], 11, v[150:151]
	s_ashr_i32 s49, s45, 31
	v_lshl_add_u64 v[146:147], s[6:7], 0, v[146:147]
	v_mov_b32_e32 v166, s49
	v_lshl_add_u64 v[146:147], v[146:147], 0, v[148:149]
	s_waitcnt vmcnt(4)
	v_pk_fma_f32 v[120:121], v[120:121], s[36:37], v[132:133] op_sel_hi:[1,0,1]
	s_waitcnt vmcnt(3)
	v_pk_fma_f32 v[124:125], v[124:125], s[36:37], v[140:141] op_sel_hi:[1,0,1]
	s_waitcnt vmcnt(2)
	v_pk_fma_f32 v[112:113], v[112:113], s[36:37], v[128:129] op_sel_hi:[1,0,1]
	s_waitcnt vmcnt(1)
	v_pk_fma_f32 v[116:117], v[116:117], s[36:37], v[136:137] op_sel_hi:[1,0,1]
	v_pk_fma_f32 v[126:127], v[126:127], s[36:37], v[142:143] op_sel_hi:[1,0,1]
	s_waitcnt vmcnt(0)
	v_mul_f32_e32 v144, 0x41800000, v161
	v_pk_mul_f32 v[124:125], v[124:125], v[144:145] op_sel_hi:[1,0]
	v_pk_mul_f32 v[120:121], v[120:121], v[144:145] op_sel_hi:[1,0]
	v_pk_mul_f32 v[116:117], v[116:117], v[144:145] op_sel_hi:[1,0]
	v_pk_mul_f32 v[112:113], v[112:113], v[144:145] op_sel_hi:[1,0]
	v_cvt_pk_fp8_f32 v162, v124, v125
	v_cvt_pk_fp8_f32 v163, v120, v121
	v_cvt_pk_fp8_f32 v164, v116, v117
	v_cvt_pk_fp8_f32 v165, v112, v113
	v_pk_fma_f32 v[122:123], v[122:123], s[36:37], v[134:135] op_sel_hi:[1,0,1]
	v_pk_fma_f32 v[118:119], v[118:119], s[36:37], v[138:139] op_sel_hi:[1,0,1]
	v_pk_fma_f32 v[114:115], v[114:115], s[36:37], v[130:131] op_sel_hi:[1,0,1]
	v_pk_mul_f32 v[126:127], v[126:127], v[144:145] op_sel_hi:[1,0]
	v_pk_mul_f32 v[122:123], v[122:123], v[144:145] op_sel_hi:[1,0]
	v_pk_mul_f32 v[118:119], v[118:119], v[144:145] op_sel_hi:[1,0]
	v_pk_mul_f32 v[114:115], v[114:115], v[144:145] op_sel_hi:[1,0]
	v_cvt_pk_fp8_f32 v162, v126, v127 op_sel:[0,0,1]
	v_cvt_pk_fp8_f32 v163, v122, v123 op_sel:[0,0,1]
	v_cvt_pk_fp8_f32 v164, v118, v119 op_sel:[0,0,1]
	v_cvt_pk_fp8_f32 v165, v114, v115 op_sel:[0,0,1]
	v_subrev_co_u32_e32 v112, vcc, s45, v150
	global_store_dwordx2 v[146:147], v[162:163], off
	global_store_dwordx2 v[146:147], v[164:165], off offset:128
	v_subb_co_u32_e32 v113, vcc, v151, v166, vcc
	v_lshl_add_u64 v[112:113], v[112:113], 2, s[56:57]
	v_mov_b32_e32 v120, v240
	v_pk_fma_f32 v[108:109], v[108:109], s[36:37], v[140:141] op_sel_hi:[1,0,1]
	v_pk_fma_f32 v[104:105], v[104:105], s[36:37], v[132:133] op_sel_hi:[1,0,1]
	v_mov_b32_e32 v114, v145
	v_mov_b32_e32 v115, v145
	v_pk_fma_f32 v[100:101], v[100:101], s[36:37], v[136:137] op_sel_hi:[1,0,1]
	v_pk_fma_f32 v[96:97], v[96:97], s[36:37], v[128:129] op_sel_hi:[1,0,1]
	v_mov_b32_e32 v116, v145
	v_mov_b32_e32 v117, v145
	v_pk_fma_f32 v[110:111], v[110:111], s[36:37], v[142:143] op_sel_hi:[1,0,1]
	v_pk_fma_f32 v[106:107], v[106:107], s[36:37], v[134:135] op_sel_hi:[1,0,1]
	v_or_b32_e32 v118, 16, v150
	v_pk_fma_f32 v[102:103], v[102:103], s[36:37], v[138:139] op_sel_hi:[1,0,1]
	v_pk_fma_f32 v[98:99], v[98:99], s[36:37], v[130:131] op_sel_hi:[1,0,1]
	v_ashrrev_i32_e32 v119, 31, v118
	v_lshlrev_b64 v[118:119], 11, v[118:119]
	v_pk_fma_f32 v[92:93], v[92:93], s[36:37], v[140:141] op_sel_hi:[1,0,1]
	v_pk_fma_f32 v[88:89], v[88:89], s[36:37], v[132:133] op_sel_hi:[1,0,1]
	v_pk_fma_f32 v[84:85], v[84:85], s[36:37], v[136:137] op_sel_hi:[1,0,1]
	v_pk_fma_f32 v[80:81], v[80:81], s[36:37], v[128:129] op_sel_hi:[1,0,1]
	v_pk_fma_f32 v[94:95], v[94:95], s[36:37], v[142:143] op_sel_hi:[1,0,1]
	v_pk_fma_f32 v[90:91], v[90:91], s[36:37], v[134:135] op_sel_hi:[1,0,1]
	v_pk_fma_f32 v[86:87], v[86:87], s[36:37], v[138:139] op_sel_hi:[1,0,1]
	v_pk_fma_f32 v[82:83], v[82:83], s[36:37], v[130:131] op_sel_hi:[1,0,1]
	v_pk_fma_f32 v[76:77], v[76:77], s[36:37], v[140:141] op_sel_hi:[1,0,1]
	v_pk_fma_f32 v[72:73], v[72:73], s[36:37], v[132:133] op_sel_hi:[1,0,1]
	v_pk_fma_f32 v[68:69], v[68:69], s[36:37], v[136:137] op_sel_hi:[1,0,1]
	v_pk_fma_f32 v[64:65], v[64:65], s[36:37], v[128:129] op_sel_hi:[1,0,1]
	v_pk_fma_f32 v[78:79], v[78:79], s[36:37], v[142:143] op_sel_hi:[1,0,1]
	v_pk_fma_f32 v[74:75], v[74:75], s[36:37], v[134:135] op_sel_hi:[1,0,1]
	v_pk_fma_f32 v[70:71], v[70:71], s[36:37], v[138:139] op_sel_hi:[1,0,1]
	v_pk_fma_f32 v[66:67], v[66:67], s[36:37], v[130:131] op_sel_hi:[1,0,1]
; __device__ __forceinline__ unsigned cvt_pk4_fp8(float a, float b, float c, float d) { int w; asm("" : "=v"(w));     w = __builtin_amdgcn_cvt_pk_fp8_f32(a, b, w, false); w = __builtin_amdgcn_cvt_pk_fp8_f32(c, d, w, true); return (unsigned)w; }
;     __device__ __forceinline__ void operator()(const f32x4 (&acc)[2][2][4][2], const Unit& u, int wr, int wc, int fr, int fq) const {
;     ...
;             for (int m = 0; m < 4; ++m) { const int r = row0 + ai * HALF + m * 16; const float rw = row_w[(size_t)u.e * XCAP + u.lr0 + (r - u.pm * BM)] * Y8_SCALE; unsigned char* rowp = O + (size_t)r * DM + col0;
; #pragma unroll
;                 for (int bj = 0; bj < 2; ++bj) { const f32x4 v0 = (acc[ai][bj][m][0] * (1.0f / (W8_SCALE * ACT8_SCALE)) + bv[bj][0]) * rw, v1 = (acc[ai][bj][m][1] * (1.0f / (W8_SCALE * ACT8_SCALE)) + bv[bj][1]) * rw;
;                     u32x2 w; w.x = cvt_pk4_fp8(v0[0], v0[1], v0[2], v0[3]); w.y = cvt_pk4_fp8(v1[0], v1[1], v1[2], v1[3]);
;                     *(u32x2*)(rowp + bj * HALF) = w; } }
	v_pk_fma_f32 v[60:61], v[60:61], s[36:37], v[140:141] op_sel_hi:[1,0,1]
	v_pk_fma_f32 v[56:57], v[56:57], s[36:37], v[132:133] op_sel_hi:[1,0,1]
	v_pk_fma_f32 v[52:53], v[52:53], s[36:37], v[136:137] op_sel_hi:[1,0,1]
	v_pk_fma_f32 v[48:49], v[48:49], s[36:37], v[128:129] op_sel_hi:[1,0,1]
	v_pk_fma_f32 v[62:63], v[62:63], s[36:37], v[142:143] op_sel_hi:[1,0,1]
	v_pk_fma_f32 v[58:59], v[58:59], s[36:37], v[134:135] op_sel_hi:[1,0,1]
	v_pk_fma_f32 v[54:55], v[54:55], s[36:37], v[138:139] op_sel_hi:[1,0,1]
	v_pk_fma_f32 v[50:51], v[50:51], s[36:37], v[130:131] op_sel_hi:[1,0,1]
	v_pk_fma_f32 v[44:45], v[44:45], s[36:37], v[140:141] op_sel_hi:[1,0,1]
	v_pk_fma_f32 v[40:41], v[40:41], s[36:37], v[132:133] op_sel_hi:[1,0,1]
	v_pk_fma_f32 v[36:37], v[36:37], s[36:37], v[136:137] op_sel_hi:[1,0,1]
	v_pk_fma_f32 v[32:33], v[32:33], s[36:37], v[128:129] op_sel_hi:[1,0,1]
	v_pk_fma_f32 v[46:47], v[46:47], s[36:37], v[142:143] op_sel_hi:[1,0,1]
	v_pk_fma_f32 v[42:43], v[42:43], s[36:37], v[134:135] op_sel_hi:[1,0,1]
	v_pk_fma_f32 v[38:39], v[38:39], s[36:37], v[138:139] op_sel_hi:[1,0,1]
	v_pk_fma_f32 v[34:35], v[34:35], s[36:37], v[130:131] op_sel_hi:[1,0,1]
	v_pk_fma_f32 v[28:29], v[28:29], s[36:37], v[140:141] op_sel_hi:[1,0,1]
	v_pk_fma_f32 v[24:25], v[24:25], s[36:37], v[132:133] op_sel_hi:[1,0,1]
	v_pk_fma_f32 v[20:21], v[20:21], s[36:37], v[136:137] op_sel_hi:[1,0,1]
	v_pk_fma_f32 v[16:17], v[16:17], s[36:37], v[128:129] op_sel_hi:[1,0,1]
	v_pk_fma_f32 v[30:31], v[30:31], s[36:37], v[142:143] op_sel_hi:[1,0,1]
	v_pk_fma_f32 v[26:27], v[26:27], s[36:37], v[134:135] op_sel_hi:[1,0,1]
	v_pk_fma_f32 v[22:23], v[22:23], s[36:37], v[138:139] op_sel_hi:[1,0,1]
	v_pk_fma_f32 v[18:19], v[18:19], s[36:37], v[130:131] op_sel_hi:[1,0,1]
	v_pk_fma_f32 v[12:13], v[12:13], s[36:37], v[140:141] op_sel_hi:[1,0,1]
	v_pk_fma_f32 v[8:9], v[8:9], s[36:37], v[132:133] op_sel_hi:[1,0,1]
	v_pk_fma_f32 v[4:5], v[4:5], s[36:37], v[136:137] op_sel_hi:[1,0,1]
	v_pk_fma_f32 v[0:1], v[0:1], s[36:37], v[128:129] op_sel_hi:[1,0,1]
	v_mov_b32_e32 v144, v145
	v_pk_fma_f32 v[14:15], v[14:15], s[36:37], v[142:143] op_sel_hi:[1,0,1]
	v_pk_fma_f32 v[10:11], v[10:11], s[36:37], v[134:135] op_sel_hi:[1,0,1]
	v_pk_fma_f32 v[6:7], v[6:7], s[36:37], v[138:139] op_sel_hi:[1,0,1]
	v_pk_fma_f32 v[2:3], v[2:3], s[36:37], v[130:131] op_sel_hi:[1,0,1]
	v_mul_f32_e32 v120, 0x41800000, v120
	v_pk_mul_f32 v[108:109], v[108:109], v[120:121] op_sel_hi:[1,0]
	v_pk_mul_f32 v[104:105], v[104:105], v[120:121] op_sel_hi:[1,0]
	v_pk_mul_f32 v[100:101], v[100:101], v[120:121] op_sel_hi:[1,0]
	v_pk_mul_f32 v[96:97], v[96:97], v[120:121] op_sel_hi:[1,0]
	v_cvt_pk_fp8_f32 v114, v108, v109
	v_cvt_pk_fp8_f32 v115, v104, v105
	v_cvt_pk_fp8_f32 v116, v100, v101
	v_cvt_pk_fp8_f32 v117, v96, v97
	v_pk_mul_f32 v[110:111], v[110:111], v[120:121] op_sel_hi:[1,0]
	v_pk_mul_f32 v[106:107], v[106:107], v[120:121] op_sel_hi:[1,0]
	v_pk_mul_f32 v[102:103], v[102:103], v[120:121] op_sel_hi:[1,0]
	v_pk_mul_f32 v[98:99], v[98:99], v[120:121] op_sel_hi:[1,0]
	v_cvt_pk_fp8_f32 v114, v110, v111 op_sel:[0,0,1]
	v_cvt_pk_fp8_f32 v115, v106, v107 op_sel:[0,0,1]
	v_cvt_pk_fp8_f32 v116, v102, v103 op_sel:[0,0,1]
	v_cvt_pk_fp8_f32 v117, v98, v99 op_sel:[0,0,1]
	v_lshl_add_u64 v[96:97], s[6:7], 0, v[118:119]
	v_lshl_add_u64 v[96:97], v[96:97], 0, v[148:149]
	global_store_dwordx2 v[96:97], v[114:115], off
	global_store_dwordx2 v[96:97], v[116:117], off offset:128
	v_mov_b32_e32 v102, v241
	v_mov_b32_e32 v96, v145
	v_mov_b32_e32 v97, v145
	v_mov_b32_e32 v98, v145
	v_mov_b32_e32 v99, v145
	v_or_b32_e32 v100, 32, v150
	v_ashrrev_i32_e32 v101, 31, v100
	v_lshlrev_b64 v[100:101], 11, v[100:101]
	v_mul_f32_e32 v102, 0x41800000, v102
	v_pk_mul_f32 v[92:93], v[92:93], v[102:103] op_sel_hi:[1,0]
	v_pk_mul_f32 v[88:89], v[88:89], v[102:103] op_sel_hi:[1,0]
	v_pk_mul_f32 v[84:85], v[84:85], v[102:103] op_sel_hi:[1,0]
	v_pk_mul_f32 v[80:81], v[80:81], v[102:103] op_sel_hi:[1,0]
	v_cvt_pk_fp8_f32 v96, v92, v93
	v_cvt_pk_fp8_f32 v97, v88, v89
	v_cvt_pk_fp8_f32 v98, v84, v85
	v_cvt_pk_fp8_f32 v99, v80, v81
	v_pk_mul_f32 v[94:95], v[94:95], v[102:103] op_sel_hi:[1,0]
	v_pk_mul_f32 v[90:91], v[90:91], v[102:103] op_sel_hi:[1,0]
	v_pk_mul_f32 v[86:87], v[86:87], v[102:103] op_sel_hi:[1,0]
	v_pk_mul_f32 v[82:83], v[82:83], v[102:103] op_sel_hi:[1,0]
	v_cvt_pk_fp8_f32 v96, v94, v95 op_sel:[0,0,1]
	v_cvt_pk_fp8_f32 v97, v90, v91 op_sel:[0,0,1]
	v_cvt_pk_fp8_f32 v98, v86, v87 op_sel:[0,0,1]
	v_cvt_pk_fp8_f32 v99, v82, v83 op_sel:[0,0,1]
	v_lshl_add_u64 v[80:81], s[6:7], 0, v[100:101]
	v_lshl_add_u64 v[80:81], v[80:81], 0, v[148:149]
	global_store_dwordx2 v[80:81], v[96:97], off
	global_store_dwordx2 v[80:81], v[98:99], off offset:128
	v_mov_b32_e32 v86, v242
	v_mov_b32_e32 v80, v145
	v_mov_b32_e32 v81, v145
	v_mov_b32_e32 v82, v145
	v_mov_b32_e32 v83, v145
	v_or_b32_e32 v84, 48, v150
	v_ashrrev_i32_e32 v85, 31, v84
	v_lshlrev_b64 v[84:85], 11, v[84:85]
	v_mul_f32_e32 v86, 0x41800000, v86
	v_pk_mul_f32 v[76:77], v[76:77], v[86:87] op_sel_hi:[1,0]
	v_pk_mul_f32 v[72:73], v[72:73], v[86:87] op_sel_hi:[1,0]
	v_pk_mul_f32 v[68:69], v[68:69], v[86:87] op_sel_hi:[1,0]
	v_pk_mul_f32 v[64:65], v[64:65], v[86:87] op_sel_hi:[1,0]
	v_cvt_pk_fp8_f32 v80, v76, v77
	v_cvt_pk_fp8_f32 v81, v72, v73
	v_cvt_pk_fp8_f32 v82, v68, v69
	v_cvt_pk_fp8_f32 v83, v64, v65
	v_pk_mul_f32 v[78:79], v[78:79], v[86:87] op_sel_hi:[1,0]
; __device__ __forceinline__ unsigned cvt_pk4_fp8(float a, float b, float c, float d) { int w; asm("" : "=v"(w));     w = __builtin_amdgcn_cvt_pk_fp8_f32(a, b, w, false); w = __builtin_amdgcn_cvt_pk_fp8_f32(c, d, w, true); return (unsigned)w; }
; #define PG8_BAR __builtin_amdgcn_s_barrier()
;     __device__ __forceinline__ void operator()(const f32x4 (&acc)[2][2][4][2], const Unit& u, int wr, int wc, int fr, int fq) const {
;     ...
;             for (int m = 0; m < 4; ++m) { const int r = row0 + ai * HALF + m * 16; const float rw = row_w[(size_t)u.e * XCAP + u.lr0 + (r - u.pm * BM)] * Y8_SCALE; unsigned char* rowp = O + (size_t)r * DM + col0;
; #pragma unroll
;                 for (int bj = 0; bj < 2; ++bj) { const f32x4 v0 = (acc[ai][bj][m][0] * (1.0f / (W8_SCALE * ACT8_SCALE)) + bv[bj][0]) * rw, v1 = (acc[ai][bj][m][1] * (1.0f / (W8_SCALE * ACT8_SCALE)) + bv[bj][1]) * rw;
;                     u32x2 w; w.x = cvt_pk4_fp8(v0[0], v0[1], v0[2], v0[3]); w.y = cvt_pk4_fp8(v1[0], v1[1], v1[2], v1[3]);
;                     *(u32x2*)(rowp + bj * HALF) = w; } }
; template <bool FP8 = false, class Epi, class Sched>
; __device__ __forceinline__ void gemm_phase(LAS unsigned char* lds, const int K, const int lda, const int ldb, const Sched& S, const Epi& E, const int wid) {
;     ...
;         if (!has_next) break;
; #pragma unroll
;         for (int a = 0; a < 2; ++a)
; #pragma unroll
;             for (int b = 0; b < 2; ++b)
; #pragma unroll
;                 for (int m = 0; m < 4; ++m)
; #pragma unroll
;                     for (int n = 0; n < 2; ++n) acc[a][b][m][n] = (f32x4){0.f, 0.f, 0.f, 0.f};
;         cur = nxt; cA = nA; cB = nB; ++ui;
;         if (wr == 1) PG8_BAR;
	v_pk_mul_f32 v[74:75], v[74:75], v[86:87] op_sel_hi:[1,0]
	v_pk_mul_f32 v[70:71], v[70:71], v[86:87] op_sel_hi:[1,0]
	v_pk_mul_f32 v[66:67], v[66:67], v[86:87] op_sel_hi:[1,0]
	v_cvt_pk_fp8_f32 v80, v78, v79 op_sel:[0,0,1]
	v_cvt_pk_fp8_f32 v81, v74, v75 op_sel:[0,0,1]
	v_cvt_pk_fp8_f32 v82, v70, v71 op_sel:[0,0,1]
	v_cvt_pk_fp8_f32 v83, v66, v67 op_sel:[0,0,1]
	v_lshl_add_u64 v[64:65], s[6:7], 0, v[84:85]
	v_lshl_add_u64 v[64:65], v[64:65], 0, v[148:149]
	global_store_dwordx2 v[64:65], v[80:81], off
	global_store_dwordx2 v[64:65], v[82:83], off offset:128
	v_mov_b32_e32 v70, v243
	v_mov_b32_e32 v64, v145
	v_mov_b32_e32 v65, v145
	v_mov_b32_e32 v66, v145
	v_mov_b32_e32 v67, v145
	v_lshl_add_u64 v[68:69], v[146:147], 0, s[12:13]
	v_mul_f32_e32 v70, 0x41800000, v70
	v_pk_mul_f32 v[60:61], v[60:61], v[70:71] op_sel_hi:[1,0]
	v_pk_mul_f32 v[56:57], v[56:57], v[70:71] op_sel_hi:[1,0]
	v_pk_mul_f32 v[52:53], v[52:53], v[70:71] op_sel_hi:[1,0]
	v_pk_mul_f32 v[48:49], v[48:49], v[70:71] op_sel_hi:[1,0]
	v_cvt_pk_fp8_f32 v64, v60, v61
	v_cvt_pk_fp8_f32 v65, v56, v57
	v_cvt_pk_fp8_f32 v66, v52, v53
	v_cvt_pk_fp8_f32 v67, v48, v49
	v_pk_mul_f32 v[62:63], v[62:63], v[70:71] op_sel_hi:[1,0]
	v_pk_mul_f32 v[58:59], v[58:59], v[70:71] op_sel_hi:[1,0]
	v_pk_mul_f32 v[54:55], v[54:55], v[70:71] op_sel_hi:[1,0]
	v_pk_mul_f32 v[50:51], v[50:51], v[70:71] op_sel_hi:[1,0]
	v_cvt_pk_fp8_f32 v64, v62, v63 op_sel:[0,0,1]
	v_cvt_pk_fp8_f32 v65, v58, v59 op_sel:[0,0,1]
	v_cvt_pk_fp8_f32 v66, v54, v55 op_sel:[0,0,1]
	v_cvt_pk_fp8_f32 v67, v50, v51 op_sel:[0,0,1]
	v_add_co_u32_e32 v48, vcc, s83, v146
	v_mov_b32_e32 v50, v145
	s_nop 0
	v_addc_co_u32_e32 v49, vcc, 0, v147, vcc
	global_store_dwordx2 v[48:49], v[64:65], off
	global_store_dwordx2 v[68:69], v[66:67], off offset:128
	v_mov_b32_e32 v54, v244
	v_mov_b32_e32 v48, v145
	v_mov_b32_e32 v49, v145
	v_mov_b32_e32 v51, v145
	v_lshl_add_u64 v[52:53], v[146:147], 0, s[38:39]
	v_mul_f32_e32 v54, 0x41800000, v54
	v_pk_mul_f32 v[44:45], v[44:45], v[54:55] op_sel_hi:[1,0]
	v_pk_mul_f32 v[40:41], v[40:41], v[54:55] op_sel_hi:[1,0]
	v_pk_mul_f32 v[36:37], v[36:37], v[54:55] op_sel_hi:[1,0]
	v_pk_mul_f32 v[32:33], v[32:33], v[54:55] op_sel_hi:[1,0]
	v_cvt_pk_fp8_f32 v48, v44, v45
	v_cvt_pk_fp8_f32 v49, v40, v41
	v_cvt_pk_fp8_f32 v50, v36, v37
	v_cvt_pk_fp8_f32 v51, v32, v33
	v_pk_mul_f32 v[46:47], v[46:47], v[54:55] op_sel_hi:[1,0]
	v_pk_mul_f32 v[42:43], v[42:43], v[54:55] op_sel_hi:[1,0]
	v_pk_mul_f32 v[38:39], v[38:39], v[54:55] op_sel_hi:[1,0]
	v_pk_mul_f32 v[34:35], v[34:35], v[54:55] op_sel_hi:[1,0]
	v_cvt_pk_fp8_f32 v48, v46, v47 op_sel:[0,0,1]
	v_cvt_pk_fp8_f32 v49, v42, v43 op_sel:[0,0,1]
	v_cvt_pk_fp8_f32 v50, v38, v39 op_sel:[0,0,1]
	v_cvt_pk_fp8_f32 v51, v34, v35 op_sel:[0,0,1]
	v_add_co_u32_e32 v32, vcc, s84, v146
	v_mov_b32_e32 v34, v145
	s_nop 0
	v_addc_co_u32_e32 v33, vcc, 0, v147, vcc
	global_store_dwordx2 v[32:33], v[48:49], off
	global_store_dwordx2 v[52:53], v[50:51], off offset:128
	v_mov_b32_e32 v38, v245
	v_mov_b32_e32 v32, v145
	v_mov_b32_e32 v33, v145
	v_mov_b32_e32 v35, v145
	v_lshl_add_u64 v[36:37], v[146:147], 0, s[40:41]
	v_mul_f32_e32 v38, 0x41800000, v38
	v_pk_mul_f32 v[28:29], v[28:29], v[38:39] op_sel_hi:[1,0]
	v_pk_mul_f32 v[24:25], v[24:25], v[38:39] op_sel_hi:[1,0]
	v_pk_mul_f32 v[20:21], v[20:21], v[38:39] op_sel_hi:[1,0]
	v_pk_mul_f32 v[16:17], v[16:17], v[38:39] op_sel_hi:[1,0]
	v_cvt_pk_fp8_f32 v32, v28, v29
	v_cvt_pk_fp8_f32 v33, v24, v25
	v_cvt_pk_fp8_f32 v34, v20, v21
	v_cvt_pk_fp8_f32 v35, v16, v17
	v_pk_mul_f32 v[30:31], v[30:31], v[38:39] op_sel_hi:[1,0]
	v_pk_mul_f32 v[26:27], v[26:27], v[38:39] op_sel_hi:[1,0]
	v_pk_mul_f32 v[22:23], v[22:23], v[38:39] op_sel_hi:[1,0]
	v_pk_mul_f32 v[18:19], v[18:19], v[38:39] op_sel_hi:[1,0]
	v_cvt_pk_fp8_f32 v32, v30, v31 op_sel:[0,0,1]
	v_cvt_pk_fp8_f32 v33, v26, v27 op_sel:[0,0,1]
	v_cvt_pk_fp8_f32 v34, v22, v23 op_sel:[0,0,1]
	v_cvt_pk_fp8_f32 v35, v18, v19 op_sel:[0,0,1]
	v_add_co_u32_e32 v16, vcc, s85, v146
	v_lshl_add_u64 v[18:19], v[146:147], 0, s[42:43]
	s_nop 0
	v_addc_co_u32_e32 v17, vcc, 0, v147, vcc
	global_store_dwordx2 v[16:17], v[32:33], off
	global_store_dwordx2 v[36:37], v[34:35], off offset:128
	v_mov_b32_e32 v20, v246
	v_mov_b32_e32 v16, v145
	v_mov_b32_e32 v17, v145
	v_mul_f32_e32 v20, 0x41800000, v20
	v_pk_mul_f32 v[12:13], v[12:13], v[20:21] op_sel_hi:[1,0]
	v_pk_mul_f32 v[8:9], v[8:9], v[20:21] op_sel_hi:[1,0]
	v_pk_mul_f32 v[4:5], v[4:5], v[20:21] op_sel_hi:[1,0]
	v_pk_mul_f32 v[0:1], v[0:1], v[20:21] op_sel_hi:[1,0]
	v_cvt_pk_fp8_f32 v16, v12, v13
	v_cvt_pk_fp8_f32 v17, v8, v9
	v_cvt_pk_fp8_f32 v144, v4, v5
	v_cvt_pk_fp8_f32 v145, v0, v1
	v_pk_mul_f32 v[14:15], v[14:15], v[20:21] op_sel_hi:[1,0]
	v_pk_mul_f32 v[10:11], v[10:11], v[20:21] op_sel_hi:[1,0]
	v_pk_mul_f32 v[6:7], v[6:7], v[20:21] op_sel_hi:[1,0]
	v_pk_mul_f32 v[2:3], v[2:3], v[20:21] op_sel_hi:[1,0]
	v_cvt_pk_fp8_f32 v16, v14, v15 op_sel:[0,0,1]
	v_cvt_pk_fp8_f32 v17, v10, v11 op_sel:[0,0,1]
	v_cvt_pk_fp8_f32 v144, v6, v7 op_sel:[0,0,1]
	v_cvt_pk_fp8_f32 v145, v2, v3 op_sel:[0,0,1]
	v_add_co_u32_e32 v0, vcc, s86, v146
	s_nop 1
	v_addc_co_u32_e32 v1, vcc, 0, v147, vcc
	s_andn2_b64 vcc, exec, s[46:47]
	s_mov_b64 s[46:47], -1
	global_store_dwordx2 v[0:1], v[16:17], off
	global_store_dwordx2 v[18:19], v[144:145], off offset:128
	s_cbranch_vccnz .LBB0_1129
	s_andn2_b64 vcc, exec, s[24:25]
	s_cbranch_vccnz .LBB0_1128
	s_barrier
	s_branch .LBB0_1128
